# gcn layer 2: removed the redundant second zero-initialisation of the 28 still-zero accumulator registers in the fast-path setup
# baseline (speedup 1.0000x reference)
.LBB5_16:
	v_cmp_ne_u32_e32 vcc, 0, v1
	v_lshlrev_b32_e32 v87, 4, v79
	v_add_u32_e32 v66, 0x5900, v3
	v_and_b32_e32 v85, 63, v78
	v_and_b32_e32 v86, 15, v78
	v_bfe_u32 v83, v78, 4, 2
	s_cbranch_vccz .LBB5_42
	v_sub_u32_e32 v0, v65, v64
	v_or_b32_e32 v88, v87, v86
	v_add_u32_e32 v91, v0, v2
	v_lshlrev_b32_e32 v90, 2, v88
	ds_read_b32 v84, v90 offset:22528
	v_add_u32_e32 v0, 15, v91
	v_ashrrev_i32_e32 v92, 4, v0
	v_add_u32_e32 v0, 2, v92
	v_ashrrev_i32_e32 v93, 1, v0
	v_cmp_gt_i32_e32 vcc, 1, v93
	v_lshlrev_b32_e32 v89, 2, v83
	s_and_saveexec_b64 s[4:5], vcc
	s_xor_b64 s[4:5], exec, s[4:5]
	v_lshlrev_b32_e32 v89, 2, v83
	s_or_saveexec_b64 s[6:7], s[4:5]
	v_mov_b32_e32 v3, 0
	v_mov_b32_e32 v2, v3
	v_mov_b32_e32 v1, v3
	v_mov_b32_e32 v0, v3
	v_mov_b32_e32 v7, v3
	v_mov_b32_e32 v6, v3
	v_mov_b32_e32 v5, v3
	v_mov_b32_e32 v4, v3
	v_mov_b32_e32 v11, v3
	v_mov_b32_e32 v10, v3
	v_mov_b32_e32 v9, v3
	v_mov_b32_e32 v8, v3
	v_mov_b32_e32 v15, v3
	v_mov_b32_e32 v14, v3
	v_mov_b32_e32 v13, v3
	v_mov_b32_e32 v12, v3
	v_mov_b32_e32 v19, v3
	v_mov_b32_e32 v18, v3
	v_mov_b32_e32 v17, v3
	v_mov_b32_e32 v16, v3
	v_mov_b32_e32 v23, v3
	v_mov_b32_e32 v22, v3
	v_mov_b32_e32 v21, v3
	v_mov_b32_e32 v20, v3
	v_mov_b32_e32 v27, v3
	v_mov_b32_e32 v26, v3
	v_mov_b32_e32 v25, v3
	v_mov_b32_e32 v24, v3
	v_mov_b32_e32 v31, v3
	v_mov_b32_e32 v30, v3
	v_mov_b32_e32 v29, v3
	v_mov_b32_e32 v28, v3
	s_xor_b64 exec, exec, s[6:7]
	s_cbranch_execz .LBB5_44
	v_lshlrev_b32_e32 v0, 4, v85
	v_mov_b32_e32 v1, 0
	v_lshl_add_u64 v[2:3], s[12:13], 0, v[0:1]
	s_movk_i32 s4, 0x1000
	v_lshlrev_b32_e32 v4, 2, v86
	v_add_co_u32_e32 v2, vcc, s4, v2
	global_load_dwordx4 v[32:35], v0, s[12:13]
	global_load_dwordx4 v[36:39], v0, s[12:13] offset:1024
	global_load_dwordx4 v[40:43], v0, s[12:13] offset:2048
	global_load_dwordx4 v[44:47], v0, s[12:13] offset:3072
	v_addc_co_u32_e32 v3, vcc, 0, v3, vcc
	global_load_dword v65, v4, s[14:15]
	global_load_dword v94, v4, s[14:15] offset:64
	global_load_dword v95, v4, s[14:15] offset:128
	global_load_dword v96, v4, s[14:15] offset:192
	global_load_dword v97, v4, s[14:15] offset:256
	global_load_dword v98, v4, s[14:15] offset:320
	global_load_dword v99, v4, s[14:15] offset:384
	global_load_dword v100, v4, s[14:15] offset:448
	global_load_dwordx4 v[48:51], v[2:3], off
	global_load_dwordx4 v[52:55], v[2:3], off offset:1024
	global_load_dwordx4 v[56:59], v[2:3], off offset:2048
	global_load_dwordx4 v[60:63], v[2:3], off offset:3072
	ds_read2st64_b32 v[2:3], v90 offset0:89 offset1:90
	ds_read_b32 v0, v66
	v_cmp_eq_u32_e32 vcc, v89, v86
	v_lshlrev_b32_e32 v4, 3, v82
	s_mov_b32 s4, 0x5040100
	s_mov_b32 s28, 0
	s_waitcnt lgkmcnt(0)
	v_sub_u32_e32 v101, v2, v0
	v_cvt_f16_f32_e32 v2, v84
	v_add_u32_e32 v102, v101, v3
	v_add_u32_e32 v3, s3, v87
	v_sub_u32_e32 v0, v64, v82
	v_or_b32_e32 v103, v3, v86
	v_mov_b32_e32 v3, 0x4400
	v_lshl_add_u32 v104, v0, 3, v3
	v_or_b32_e32 v0, 2, v89
	v_cndmask_b32_e32 v66, 0, v2, vcc
	v_or_b32_e32 v3, 1, v89
	v_cmp_eq_u32_e32 vcc, v0, v86
	s_mov_b64 s[12:13], 0
	s_mov_b32 s29, 0
	v_cndmask_b32_e32 v0, 0, v2, vcc
	v_cmp_eq_u32_e32 vcc, v3, v86
	v_or_b32_e32 v3, 3, v89
	v_mov_b32_e32 v28, v1
	v_cndmask_b32_e32 v67, 0, v2, vcc
	v_cmp_eq_u32_e32 vcc, v3, v86
	v_lshlrev_b32_e32 v3, 3, v86
	v_lshl_add_u32 v3, v64, 3, v3
	v_cndmask_b32_e32 v2, 0, v2, vcc
	v_pack_b32_f16 v105, v0, v2
	v_pack_b32_f16 v0, v67, v0
	v_sub_u32_e32 v3, v3, v4
	v_add_u32_e32 v106, 0x4400, v3
	v_alignbit_b32 v107, v2, v0, 16
	v_perm_b32 v108, v0, v66, s4
	v_mov_b32_e32 v0, v1
	v_mov_b32_e32 v2, v1
	v_mov_b32_e32 v3, v1
	v_mov_b32_e32 v4, v1
	v_and_b32_e32 v109, 48, v78
	v_add_u32_e32 v110, -1, v91
	v_add_u32_e32 v111, -1, v92
	v_pack_b32_f16 v64, v66, v67
	v_readfirstlane_b32 s40, v92
	v_sub_u32_e32 v102, v102, v101
	s_nop 3
	s_branch .LBB5_23
